# v65 + down-projection epilogue skips the stores of 32-row groups that are entirely padding rows (wave-uniform test)
# speedup vs baseline: 1.0140x; 1.0041x over previous
.LBB0_1029:
	v_bfe_i32 v2, v4, 27, 1
	v_lshlrev_b32_e32 v0, 4, v4
	v_lshrrev_b32_e32 v2, 22, v2
	v_add_u32_e32 v2, v0, v2
	v_and_b32_e32 v2, 0xfffffc00, v2
	v_sub_u32_e32 v2, v0, v2
	v_ashrrev_i32_e32 v1, 31, v4
	v_lshrrev_b32_e32 v3, 4, v2
	v_lshrrev_b32_e32 v1, 26, v1
	v_bitop3_b32 v3, v3, v2, 32 bitop3:0x6c
	v_ashrrev_i32_e32 v2, 31, v2
	v_add_u32_e32 v1, v4, v1
	v_lshrrev_b32_e32 v2, 26, v2
	v_ashrrev_i32_e32 v1, 6, v1
	v_add_u32_e32 v2, v3, v2
	s_add_u32 s21, s90, 0x4a800000
	v_lshlrev_b32_e32 v5, 3, v1
	v_ashrrev_i32_e32 v2, 6, v2
	s_addc_u32 s33, s91, 0
	v_and_b32_e32 v5, -16, v5
	v_mul_i32_i24_e32 v6, 64, v2
	s_add_u32 s6, s90, 0x14800000
	v_readlane_b32 s10, v255, 25
	v_add_u32_e32 v5, v2, v5
	v_sub_u32_e32 v3, v3, v6
	v_mov_b32_e32 v159, 1
	s_addc_u32 s7, s91, 0
	s_lshr_b32 s18, s10, 8
	v_lshlrev_b32_e32 v1, 5, v1
	v_ashrrev_i16_sdwa v3, v159, sext(v3) dst_sel:DWORD dst_unused:UNUSED_PAD src0_sel:DWORD src1_sel:BYTE_0
	v_lshlrev_b32_e32 v6, 1, v5
	v_lshrrev_b32_e32 v7, 2, v5
	v_and_b32_e32 v2, 3, v2
	s_mov_b32 s10, 0x1fffe0
	v_and_b32_e32 v1, 32, v1
	v_bfe_i32 v3, v3, 0, 16
	v_and_b32_e32 v6, 24, v6
	v_and_b32_e32 v7, 4, v7
	v_and_or_b32 v2, v5, s10, v2
	v_or3_b32 v2, v2, v7, v6
	v_add_lshl_u32 v1, v1, v3, 1
	v_add_u32_e32 v0, 0x2000, v0
	v_lshl_add_u32 v148, v2, 11, v1
	v_ashrrev_i32_e32 v1, 31, v0
	v_lshrrev_b32_e32 v1, 22, v1
	v_add_u32_e32 v1, v0, v1
	v_ashrrev_i32_e32 v1, 10, v1
	v_mul_i32_i24_e32 v2, 0x400, v1
	v_sub_u32_e32 v0, v0, v2
	v_lshrrev_b32_e32 v2, 4, v0
	v_bitop3_b32 v0, v2, v0, 32 bitop3:0x6c
	v_ashrrev_i32_e32 v3, 31, v0
	v_lshrrev_b32_e32 v3, 26, v3
	v_lshlrev_b32_e32 v2, 3, v1
	v_add_u32_e32 v3, v0, v3
	v_lshlrev_b32_e32 v1, 5, v1
	v_and_b32_e32 v6, 32, v1
	v_and_b32_e32 v1, 0xc0, v3
	v_and_b32_e32 v2, -16, v2
	v_ashrrev_i32_e32 v5, 6, v3
	v_sub_u32_e32 v0, v0, v1
	v_add_u32_e32 v2, v5, v2
	v_ashrrev_i16_sdwa v0, v159, sext(v0) dst_sel:DWORD dst_unused:UNUSED_PAD src0_sel:DWORD src1_sel:BYTE_0
	v_and_b32_e32 v5, 3, v5
	v_bfe_i32 v3, v0, 0, 16
	v_lshlrev_b32_e32 v0, 1, v2
	v_lshrrev_b32_e32 v1, 2, v2
	v_and_or_b32 v2, v2, s10, v5
	s_lshl_b32 s10, s0, 2
	s_add_i32 s10, s10, 0
	s_add_i32 s10, s10, 0x20400
	v_and_b32_e32 v0, 24, v0
	v_and_b32_e32 v1, 4, v1
	v_mov_b32_e32 v5, s10
	v_or3_b32 v2, v2, v1, v0
	ds_read2_b32 v[0:1], v5 offset0:32 offset1:64
	ds_read_b32 v100, v5
	v_add_lshl_u32 v3, v6, v3, 1
	v_lshl_add_u32 v150, v2, 11, v3
	ds_read_b32 v2, v5 offset:384
	s_lshl_b32 s48, s94, 10
	s_waitcnt lgkmcnt(1)
	v_readfirstlane_b32 s10, v0
	s_abs_i32 s11, s10
	v_cvt_f32_u32_e32 v0, s11
	s_waitcnt lgkmcnt(0)
	v_readfirstlane_b32 s12, v2
	v_readfirstlane_b32 s99, v100
	s_sub_i32 s14, 0, s11
	s_lshl_b32 s12, s12, 3
	v_rcp_iflag_f32_e32 v0, v0
	s_sub_i32 s1, s1, s12
	s_ashr_i32 s13, s1, 31
	s_abs_i32 s1, s1
	v_mul_f32_e32 v0, 0x4f7ffffe, v0
	v_cvt_u32_f32_e32 v0, v0
	s_ashr_i32 s10, s10, 31
	s_xor_b32 s10, s13, s10
	v_readfirstlane_b32 s12, v1
	v_readfirstlane_b32 s15, v0
	s_mul_i32 s14, s14, s15
	s_mul_hi_u32 s14, s15, s14
	s_add_i32 s15, s15, s14
	s_mul_hi_u32 s14, s1, s15
	s_mul_i32 s15, s14, s11
	s_sub_i32 s1, s1, s15
	s_add_i32 s15, s14, 1
	s_sub_i32 s16, s1, s11
	s_cmp_ge_u32 s1, s11
	s_cselect_b32 s14, s15, s14
	s_cselect_b32 s1, s16, s1
	s_add_i32 s15, s14, 1
	s_sub_i32 s16, s1, s11
	s_cmp_ge_u32 s1, s11
	s_cselect_b32 s1, s16, s1
	s_cselect_b32 s11, s15, s14
	s_xor_b32 s1, s1, s13
	s_sub_i32 s1, s1, s13
	s_lshl_b32 s1, s1, 8
	s_xor_b32 s11, s11, s10
	s_add_i32 s49, s1, s12
	s_sub_i32 s99, s99, s1
	s_mov_b32 s97, s99
	s_ashr_i32 s1, s0, 31
	s_sub_i32 s10, s11, s10
	s_lshl_b64 s[12:13], s[0:1], 22
	s_add_u32 s1, s21, s12
	s_addc_u32 s14, s33, s13
	s_ashr_i32 s11, s10, 31
	s_lshl_b64 s[12:13], s[10:11], 19
	s_add_u32 s12, s1, s12
	v_mbcnt_lo_u32_b32 v0, -1, 0
	v_mbcnt_hi_u32_b32 v0, -1, v0
	v_readlane_b32 s1, v255, 4
	s_addc_u32 s13, s14, s13
	s_mov_b64 s[14:15], s[12:13]
	v_add_u32_e32 v0, s1, v0
	s_add_i32 s1, s49, 0x80
	v_ashrrev_i32_e32 v2, 31, v0
	v_lshrrev_b32_e32 v2, 26, v2
	v_lshlrev_b32_e32 v1, 4, v0
	v_add_u32_e32 v2, v0, v2
	v_bfe_i32 v0, v0, 27, 1
	v_lshrrev_b32_e32 v0, 22, v0
	v_add_u32_e32 v0, v1, v0
	v_and_b32_e32 v0, 0xfffffc00, v0
	v_sub_u32_e32 v0, v1, v0
	v_lshrrev_b32_e32 v3, 4, v0
	v_bitop3_b32 v3, v3, v0, 32 bitop3:0x6c
	v_ashrrev_i32_e32 v0, 31, v0
	v_ashrrev_i32_e32 v2, 6, v2
	v_lshrrev_b32_e32 v0, 26, v0
	v_lshlrev_b32_e32 v5, 3, v2
	v_add_u32_e32 v0, v3, v0
	v_and_b32_e32 v5, -16, v5
	v_ashrrev_i32_e32 v0, 6, v0
	v_add_u32_e32 v5, v0, v5
	v_mul_i32_i24_e32 v0, 64, v0
	v_sub_u32_e32 v0, v3, v0
	v_lshlrev_b32_e32 v2, 5, v2
	v_ashrrev_i16_sdwa v0, v159, sext(v0) dst_sel:DWORD dst_unused:UNUSED_PAD src0_sel:DWORD src1_sel:BYTE_0
	v_and_b32_e32 v2, 32, v2
	v_bfe_i32 v0, v0, 0, 16
	v_add_lshl_u32 v2, v2, v0, 1
	v_cmp_gt_u32_e32 vcc, s99, v5
	s_nop 1
	v_cndmask_b32_e32 v0, 0, v5, vcc
	v_add_u32_e32 v0, s49, v0
	v_add_u32_e32 v3, 0x80, v5
	v_cmp_gt_u32_e32 vcc, s99, v3
	s_nop 1
	v_cndmask_b32_e32 v3, 0, v3, vcc
	v_add_u32_e32 v3, s49, v3
	v_add_u32_e32 v1, 0x2000, v1
	v_lshl_add_u32 v0, v0, 11, v2
	v_lshl_add_u32 v2, v3, 11, v2
	v_ashrrev_i32_e32 v3, 31, v1
	v_lshrrev_b32_e32 v3, 22, v3
	v_add_u32_e32 v3, v1, v3
	v_ashrrev_i32_e32 v3, 10, v3
	v_mul_i32_i24_e32 v5, 0x400, v3
	v_sub_u32_e32 v1, v1, v5
	v_lshrrev_b32_e32 v5, 4, v1
	v_bitop3_b32 v1, v5, v1, 32 bitop3:0x6c
	v_ashrrev_i32_e32 v6, 31, v1
	v_lshrrev_b32_e32 v6, 26, v6
	v_add_u32_e32 v6, v1, v6
	v_ashrrev_i32_e32 v7, 6, v6
	v_and_b32_e32 v6, 0xc0, v6
	v_lshlrev_b32_e32 v5, 3, v3
	v_sub_u32_e32 v1, v1, v6
	v_and_b32_e32 v5, -16, v5
	v_lshlrev_b32_e32 v3, 5, v3
	v_ashrrev_i16_sdwa v1, v159, sext(v1) dst_sel:DWORD dst_unused:UNUSED_PAD src0_sel:DWORD src1_sel:BYTE_0
	v_add_u32_e32 v5, v7, v5
	v_and_b32_e32 v3, 32, v3
	v_bfe_i32 v1, v1, 0, 16
	v_add_lshl_u32 v1, v3, v1, 1
	v_cmp_gt_u32_e32 vcc, s99, v5
	s_nop 1
	v_cndmask_b32_e32 v3, 0, v5, vcc
	v_add_u32_e32 v3, s49, v3
	v_lshl_add_u32 v152, v3, 11, v1
	v_add_u32_e32 v3, 0x80, v5
	v_cmp_gt_u32_e32 vcc, s99, v3
	s_nop 1
	v_cndmask_b32_e32 v3, 0, v3, vcc
	v_add_u32_e32 v3, s49, v3
	s_add_i32 s1, s48, 0
	s_add_i32 m0, s1, 0x10000
	v_lshl_add_u32 v3, v3, 11, v1
	global_load_lds_dwordx4 v148, s[14:15]
	s_add_i32 m0, s1, 0x12000
	v_mov_b32_e32 v149, 0
	global_load_lds_dwordx4 v150, s[14:15]
	s_add_u32 s14, s12, 0x40000
	s_addc_u32 s15, s13, 0
	s_add_i32 m0, s1, 0x14000
	s_add_i32 s11, s1, 0x2000
	global_load_lds_dwordx4 v148, s[14:15]
	s_add_i32 m0, s1, 0x16000
	s_add_i32 s50, s1, 0x4000
	global_load_lds_dwordx4 v150, s[14:15]
	s_mov_b64 s[14:15], s[6:7]
	s_mov_b32 m0, s1
	s_add_i32 s51, s1, 0x6000
	global_load_lds_dwordx4 v0, s[14:15]
	s_mov_b32 m0, s11
	s_cmp_eq_u32 s18, 1
	global_load_lds_dwordx4 v152, s[14:15]
	s_mov_b64 s[14:15], s[6:7]
	s_mov_b32 m0, s50
	s_mov_b32 s66, s60
	global_load_lds_dwordx4 v2, s[14:15]
	s_mov_b32 m0, s51
	s_mov_b32 s54, 0
	global_load_lds_dwordx4 v3, s[14:15]
	s_mov_b32 s52, 0x10000
	v_mov_b32_e32 v151, v149
	v_mov_b32_e32 v1, v149
	s_cselect_b64 s[14:15], -1, 0
	s_cmp_lg_u32 s18, 1
	v_mov_b32_e32 v153, v149
	s_cbranch_scc1 .LBB0_1031
	s_barrier

.LBB0_1032:
	s_mov_b32 s97, s98
	v_mov_b32_e32 v4, 0
	s_waitcnt lgkmcnt(0)
	v_mov_b32_e32 v152, v1
	s_mov_b32 s49, s62
	s_mov_b32 s10, s26
	s_mov_b32 s22, s24
	s_mov_b64 s[12:13], s[34:35]
	s_mov_b32 s54, s63
	v_mov_b32_e32 v5, v4
	v_mov_b32_e32 v6, v4
	v_mov_b32_e32 v7, v4
	v_mov_b32_e32 v8, v4
	v_mov_b32_e32 v9, v4
	v_mov_b32_e32 v10, v4
	v_mov_b32_e32 v11, v4
	v_mov_b32_e32 v12, v4
	v_mov_b32_e32 v13, v4
	v_mov_b32_e32 v14, v4
	v_mov_b32_e32 v15, v4
	v_mov_b32_e32 v16, v4
	v_mov_b32_e32 v17, v4
	v_mov_b32_e32 v18, v4
	v_mov_b32_e32 v19, v4
	v_mov_b32_e32 v20, v4
	v_mov_b32_e32 v21, v4
	v_mov_b32_e32 v22, v4
	v_mov_b32_e32 v23, v4
	v_mov_b32_e32 v24, v4
	v_mov_b32_e32 v25, v4
	v_mov_b32_e32 v26, v4
	v_mov_b32_e32 v27, v4
	v_mov_b32_e32 v232, v4
	v_mov_b32_e32 v233, v4
	v_mov_b32_e32 v234, v4
	v_mov_b32_e32 v235, v4
	v_mov_b32_e32 v32, v4
	v_mov_b32_e32 v33, v4
	v_mov_b32_e32 v34, v4
	v_mov_b32_e32 v35, v4
	v_mov_b32_e32 v36, v4
	v_mov_b32_e32 v37, v4
	v_mov_b32_e32 v38, v4
	v_mov_b32_e32 v39, v4
	v_mov_b32_e32 v40, v4
	v_mov_b32_e32 v41, v4
	v_mov_b32_e32 v42, v4
	v_mov_b32_e32 v43, v4
	v_mov_b32_e32 v44, v4
	v_mov_b32_e32 v45, v4
	v_mov_b32_e32 v46, v4
	v_mov_b32_e32 v47, v4
	v_mov_b32_e32 v48, v4
	v_mov_b32_e32 v49, v4
	v_mov_b32_e32 v50, v4
	v_mov_b32_e32 v51, v4
	v_mov_b32_e32 v52, v4
	v_mov_b32_e32 v53, v4
	v_mov_b32_e32 v54, v4
	v_mov_b32_e32 v55, v4
	v_mov_b32_e32 v56, v4
	v_mov_b32_e32 v57, v4
	v_mov_b32_e32 v58, v4
	v_mov_b32_e32 v59, v4
	v_mov_b32_e32 v60, v4
	v_mov_b32_e32 v61, v4
	v_mov_b32_e32 v62, v4
	v_mov_b32_e32 v63, v4
	v_mov_b32_e32 v64, v4
	v_mov_b32_e32 v65, v4
	v_mov_b32_e32 v66, v4
	v_mov_b32_e32 v67, v4
	v_mov_b32_e32 v28, v4
	v_mov_b32_e32 v29, v4
	v_mov_b32_e32 v30, v4
	v_mov_b32_e32 v31, v4
	v_mov_b32_e32 v72, v4
	v_mov_b32_e32 v73, v4
	v_mov_b32_e32 v74, v4
	v_mov_b32_e32 v75, v4
	v_mov_b32_e32 v76, v4
	v_mov_b32_e32 v77, v4
	v_mov_b32_e32 v78, v4
	v_mov_b32_e32 v79, v4
	v_mov_b32_e32 v80, v4
	v_mov_b32_e32 v81, v4
	v_mov_b32_e32 v82, v4
	v_mov_b32_e32 v83, v4
	v_mov_b32_e32 v84, v4
	v_mov_b32_e32 v85, v4
	v_mov_b32_e32 v86, v4
	v_mov_b32_e32 v87, v4
	v_mov_b32_e32 v88, v4
	v_mov_b32_e32 v89, v4
	v_mov_b32_e32 v90, v4
	v_mov_b32_e32 v91, v4
	v_mov_b32_e32 v92, v4
	v_mov_b32_e32 v93, v4
	v_mov_b32_e32 v94, v4
	v_mov_b32_e32 v95, v4
	v_mov_b32_e32 v96, v4
	v_mov_b32_e32 v97, v4
	v_mov_b32_e32 v98, v4
	v_mov_b32_e32 v99, v4
	v_mov_b32_e32 v100, v4
	v_mov_b32_e32 v101, v4
	v_mov_b32_e32 v102, v4
	v_mov_b32_e32 v103, v4
	v_mov_b32_e32 v104, v4
	v_mov_b32_e32 v105, v4
	v_mov_b32_e32 v106, v4
	v_mov_b32_e32 v107, v4
	v_mov_b32_e32 v108, v4
	v_mov_b32_e32 v109, v4
	v_mov_b32_e32 v110, v4
	v_mov_b32_e32 v111, v4
	v_mov_b32_e32 v112, v4
	v_mov_b32_e32 v113, v4
	v_mov_b32_e32 v114, v4
	v_mov_b32_e32 v115, v4
	v_mov_b32_e32 v116, v4
	v_mov_b32_e32 v117, v4
	v_mov_b32_e32 v118, v4
	v_mov_b32_e32 v119, v4
	v_mov_b32_e32 v120, v4
	v_mov_b32_e32 v121, v4
	v_mov_b32_e32 v122, v4
	v_mov_b32_e32 v123, v4
	v_mov_b32_e32 v124, v4
	v_mov_b32_e32 v125, v4
	v_mov_b32_e32 v126, v4
	v_mov_b32_e32 v127, v4
	v_mov_b32_e32 v128, v4
	v_mov_b32_e32 v129, v4
	v_mov_b32_e32 v130, v4
	v_mov_b32_e32 v131, v4

.LBB0_1050:
	s_sub_i32 s96, s97, s53
	s_lshl_b32 s23, s10, 8
	v_mbcnt_lo_u32_b32 v1, -1, 0
	v_mbcnt_hi_u32_b32 v1, -1, v1
	s_or_b32 s23, s23, s55
	v_ashrrev_i32_e32 v149, 4, v1
	v_lshl_add_u32 v154, v149, 3, s23
	s_ashr_i32 s23, s22, 31
	s_lshl_b64 s[38:39], s[22:23], 13
	s_add_u32 s38, s84, s38
	s_addc_u32 s39, s85, s39
	v_ashrrev_i32_e32 v155, 31, v154
	v_lshl_add_u64 v[68:69], v[154:155], 2, s[38:39]
	global_load_dwordx4 v[144:147], v[68:69], off
	global_load_dwordx4 v[140:143], v[68:69], off offset:16
	global_load_dwordx4 v[136:139], v[68:69], off offset:512
	global_load_dwordx4 v[132:135], v[68:69], off offset:528
	v_and_b32_e32 v149, 1, v149
	v_and_b32_e32 v1, 15, v1
	v_lshlrev_b32_e32 v156, 4, v149
	s_add_i32 s23, s49, s53
	v_add3_u32 v156, s23, v1, v156
	v_ashrrev_i32_e32 v157, 31, v156
	v_lshlrev_b32_e32 v149, 3, v149
	v_lshlrev_b64 v[156:157], 11, v[156:157]
	v_sub_co_u32_e32 v168, vcc, 0, v149
	v_lshl_add_u64 v[156:157], s[16:17], 0, v[156:157]
	s_nop 0
	v_subb_co_u32_e64 v169, s[38:39], 0, 0, vcc
	v_lshl_add_u64 v[154:155], v[156:157], 0, v[154:155]
	v_mov_b32_e32 v68, 0
	v_mov_b32_e32 v69, 0
	v_mov_b32_e32 v70, 0
	v_mov_b32_e32 v71, 0
	v_lshl_add_u64 v[154:155], v[154:155], 0, v[168:169]
	v_mov_b32_e32 v160, 0
	v_mov_b32_e32 v161, 0
	v_mov_b32_e32 v162, 0
	v_mov_b32_e32 v163, 0
	v_mov_b32_e32 v164, 0
	v_mov_b32_e32 v165, 0
	v_mov_b32_e32 v166, 0
	v_mov_b32_e32 v167, 0
	s_waitcnt vmcnt(0)
	v_pk_fma_f32 v[168:169], v[128:129], s[20:21], v[144:145] op_sel_hi:[1,0,1]
	v_pk_fma_f32 v[172:173], v[124:125], s[20:21], v[140:141] op_sel_hi:[1,0,1]
	v_pk_fma_f32 v[176:177], v[120:121], s[20:21], v[144:145] op_sel_hi:[1,0,1]
	v_pk_fma_f32 v[180:181], v[116:117], s[20:21], v[140:141] op_sel_hi:[1,0,1]
	v_pk_fma_f32 v[184:185], v[96:97], s[20:21], v[136:137] op_sel_hi:[1,0,1]
	v_pk_fma_f32 v[188:189], v[92:93], s[20:21], v[132:133] op_sel_hi:[1,0,1]
	v_pk_fma_f32 v[192:193], v[88:89], s[20:21], v[136:137] op_sel_hi:[1,0,1]
	v_pk_fma_f32 v[196:197], v[84:85], s[20:21], v[132:133] op_sel_hi:[1,0,1]
	v_pk_fma_f32 v[200:201], v[112:113], s[20:21], v[144:145] op_sel_hi:[1,0,1]
	v_pk_fma_f32 v[204:205], v[108:109], s[20:21], v[140:141] op_sel_hi:[1,0,1]
	v_pk_fma_f32 v[208:209], v[104:105], s[20:21], v[144:145] op_sel_hi:[1,0,1]
	v_pk_fma_f32 v[212:213], v[100:101], s[20:21], v[140:141] op_sel_hi:[1,0,1]
	v_cvt_pk_fp8_f32 v68, v168, v169
	v_cvt_pk_fp8_f32 v69, v172, v173
	v_cvt_pk_fp8_f32 v70, v176, v177
	v_cvt_pk_fp8_f32 v71, v180, v181
	v_cvt_pk_fp8_f32 v160, v184, v185
	v_cvt_pk_fp8_f32 v161, v188, v189
	v_cvt_pk_fp8_f32 v162, v192, v193
	v_cvt_pk_fp8_f32 v163, v196, v197
	v_cvt_pk_fp8_f32 v164, v200, v201
	v_cvt_pk_fp8_f32 v165, v204, v205
	v_cvt_pk_fp8_f32 v166, v208, v209
	v_cvt_pk_fp8_f32 v167, v212, v213
	v_pk_fma_f32 v[156:157], v[130:131], s[20:21], v[146:147] op_sel_hi:[1,0,1]
	v_pk_fma_f32 v[170:171], v[126:127], s[20:21], v[142:143] op_sel_hi:[1,0,1]
	v_pk_fma_f32 v[174:175], v[122:123], s[20:21], v[146:147] op_sel_hi:[1,0,1]
	v_pk_fma_f32 v[178:179], v[118:119], s[20:21], v[142:143] op_sel_hi:[1,0,1]
	v_pk_fma_f32 v[182:183], v[98:99], s[20:21], v[138:139] op_sel_hi:[1,0,1]
	v_pk_fma_f32 v[186:187], v[94:95], s[20:21], v[134:135] op_sel_hi:[1,0,1]
	v_pk_fma_f32 v[190:191], v[90:91], s[20:21], v[138:139] op_sel_hi:[1,0,1]
	v_pk_fma_f32 v[194:195], v[86:87], s[20:21], v[134:135] op_sel_hi:[1,0,1]
	v_pk_fma_f32 v[198:199], v[114:115], s[20:21], v[146:147] op_sel_hi:[1,0,1]
	v_pk_fma_f32 v[202:203], v[110:111], s[20:21], v[142:143] op_sel_hi:[1,0,1]
	v_pk_fma_f32 v[206:207], v[106:107], s[20:21], v[146:147] op_sel_hi:[1,0,1]
	v_pk_fma_f32 v[210:211], v[102:103], s[20:21], v[142:143] op_sel_hi:[1,0,1]
	v_cvt_pk_fp8_f32 v68, v156, v157 op_sel:[0,0,1]
	v_cvt_pk_fp8_f32 v69, v170, v171 op_sel:[0,0,1]
	v_cvt_pk_fp8_f32 v70, v174, v175 op_sel:[0,0,1]
	v_cvt_pk_fp8_f32 v71, v178, v179 op_sel:[0,0,1]
	v_cvt_pk_fp8_f32 v160, v182, v183 op_sel:[0,0,1]
	v_cvt_pk_fp8_f32 v161, v186, v187 op_sel:[0,0,1]
	v_cvt_pk_fp8_f32 v162, v190, v191 op_sel:[0,0,1]
	v_cvt_pk_fp8_f32 v163, v194, v195 op_sel:[0,0,1]
	v_cvt_pk_fp8_f32 v164, v198, v199 op_sel:[0,0,1]
	v_cvt_pk_fp8_f32 v166, v206, v207 op_sel:[0,0,1]
	v_cvt_pk_fp8_f32 v165, v202, v203 op_sel:[0,0,1]
	v_cvt_pk_fp8_f32 v167, v210, v211 op_sel:[0,0,1]
	v_permlane16_swap_b32_e32 v68, v70
	v_permlane16_swap_b32_e32 v69, v71
	v_add_co_u32_e32 v156, vcc, s52, v154
	v_permlane16_swap_b32_e32 v160, v162
	v_permlane16_swap_b32_e32 v161, v163
	s_cmp_le_i32 s96, 0
	s_cbranch_scc1 .Lp7st_0
	global_store_dwordx4 v[154:155], v[68:71], off
.Lp7st_0:
	s_cmp_le_i32 s96, 0
	s_cbranch_scc1 .Lp7st_1
	global_store_dwordx4 v[154:155], v[160:163], off offset:128
.Lp7st_1:
	v_permlane16_swap_b32_e32 v164, v166
	v_permlane16_swap_b32_e32 v165, v167
	v_addc_co_u32_e32 v157, vcc, 0, v155, vcc
	v_pk_fma_f32 v[70:71], v[80:81], s[20:21], v[136:137] op_sel_hi:[1,0,1]
	v_mov_b32_e32 v68, 0
	s_cmp_le_i32 s96, 32
	s_cbranch_scc1 .Lp7st_2
	global_store_dwordx4 v[156:157], v[164:167], off
.Lp7st_2:
	v_pk_fma_f32 v[168:169], v[72:73], s[20:21], v[136:137] op_sel_hi:[1,0,1]
	v_pk_fma_f32 v[172:173], v[28:29], s[20:21], v[132:133] op_sel_hi:[1,0,1]
	v_pk_fma_f32 v[164:165], v[76:77], s[20:21], v[132:133] op_sel_hi:[1,0,1]
	v_cvt_pk_fp8_f32 v68, v70, v71
	v_mov_b32_e32 v69, 0
	v_mov_b32_e32 v70, 0
	v_mov_b32_e32 v71, 0
	v_cvt_pk_fp8_f32 v69, v164, v165
	v_cvt_pk_fp8_f32 v70, v168, v169
	v_cvt_pk_fp8_f32 v71, v172, v173
	v_pk_fma_f32 v[160:161], v[82:83], s[20:21], v[138:139] op_sel_hi:[1,0,1]
	v_pk_fma_f32 v[162:163], v[78:79], s[20:21], v[134:135] op_sel_hi:[1,0,1]
	v_pk_fma_f32 v[166:167], v[74:75], s[20:21], v[138:139] op_sel_hi:[1,0,1]
	v_pk_fma_f32 v[170:171], v[30:31], s[20:21], v[134:135] op_sel_hi:[1,0,1]
	v_cvt_pk_fp8_f32 v68, v160, v161 op_sel:[0,0,1]
	v_cvt_pk_fp8_f32 v70, v166, v167 op_sel:[0,0,1]
	v_cvt_pk_fp8_f32 v69, v162, v163 op_sel:[0,0,1]
	v_cvt_pk_fp8_f32 v71, v170, v171 op_sel:[0,0,1]
	v_pk_fma_f32 v[162:163], v[60:61], s[20:21], v[140:141] op_sel_hi:[1,0,1]
	v_permlane16_swap_b32_e32 v68, v70
	v_permlane16_swap_b32_e32 v69, v71
	s_cmp_le_i32 s96, 32
	s_cbranch_scc1 .Lp7st_3
	global_store_dwordx4 v[156:157], v[68:71], off offset:128
.Lp7st_3:
	v_pk_fma_f32 v[166:167], v[56:57], s[20:21], v[144:145] op_sel_hi:[1,0,1]
	v_pk_fma_f32 v[170:171], v[52:53], s[20:21], v[140:141] op_sel_hi:[1,0,1]
	v_pk_fma_f32 v[70:71], v[64:65], s[20:21], v[144:145] op_sel_hi:[1,0,1]
	v_mov_b32_e32 v68, 0
	v_cvt_pk_fp8_f32 v68, v70, v71
	v_mov_b32_e32 v69, 0
	v_mov_b32_e32 v70, 0
	v_mov_b32_e32 v71, 0
	v_cvt_pk_fp8_f32 v69, v162, v163
	v_cvt_pk_fp8_f32 v70, v166, v167
	v_cvt_pk_fp8_f32 v71, v170, v171
	v_pk_fma_f32 v[156:157], v[66:67], s[20:21], v[146:147] op_sel_hi:[1,0,1]
	v_pk_fma_f32 v[160:161], v[62:63], s[20:21], v[142:143] op_sel_hi:[1,0,1]
	v_pk_fma_f32 v[164:165], v[58:59], s[20:21], v[146:147] op_sel_hi:[1,0,1]
	v_pk_fma_f32 v[168:169], v[54:55], s[20:21], v[142:143] op_sel_hi:[1,0,1]
	v_cvt_pk_fp8_f32 v68, v156, v157 op_sel:[0,0,1]
	v_cvt_pk_fp8_f32 v70, v164, v165 op_sel:[0,0,1]
	v_cvt_pk_fp8_f32 v69, v160, v161 op_sel:[0,0,1]
	v_cvt_pk_fp8_f32 v71, v168, v169 op_sel:[0,0,1]
	v_add_co_u32_e32 v156, vcc, s60, v154
	v_permlane16_swap_b32_e32 v68, v70
	v_permlane16_swap_b32_e32 v69, v71
	v_addc_co_u32_e32 v157, vcc, 0, v155, vcc
	s_cmp_le_i32 s96, 128
	s_cbranch_scc1 .Lp7st_4
	global_store_dwordx4 v[156:157], v[68:71], off
.Lp7st_4:
	v_pk_fma_f32 v[164:165], v[232:233], s[20:21], v[132:133] op_sel_hi:[1,0,1]
	v_pk_fma_f32 v[168:169], v[24:25], s[20:21], v[136:137] op_sel_hi:[1,0,1]
	v_pk_fma_f32 v[70:71], v[32:33], s[20:21], v[136:137] op_sel_hi:[1,0,1]
	v_mov_b32_e32 v68, 0
	v_pk_fma_f32 v[172:173], v[20:21], s[20:21], v[132:133] op_sel_hi:[1,0,1]
	v_cvt_pk_fp8_f32 v68, v70, v71
	v_mov_b32_e32 v69, 0
	v_mov_b32_e32 v70, 0
	v_mov_b32_e32 v71, 0
	v_cvt_pk_fp8_f32 v69, v164, v165
	v_cvt_pk_fp8_f32 v70, v168, v169
	v_cvt_pk_fp8_f32 v71, v172, v173
	v_pk_fma_f32 v[160:161], v[34:35], s[20:21], v[138:139] op_sel_hi:[1,0,1]
	v_pk_fma_f32 v[162:163], v[234:235], s[20:21], v[134:135] op_sel_hi:[1,0,1]
	v_pk_fma_f32 v[166:167], v[26:27], s[20:21], v[138:139] op_sel_hi:[1,0,1]
	v_pk_fma_f32 v[170:171], v[22:23], s[20:21], v[134:135] op_sel_hi:[1,0,1]
	v_cvt_pk_fp8_f32 v68, v160, v161 op_sel:[0,0,1]
	v_cvt_pk_fp8_f32 v70, v166, v167 op_sel:[0,0,1]
	v_cvt_pk_fp8_f32 v69, v162, v163 op_sel:[0,0,1]
	v_cvt_pk_fp8_f32 v71, v170, v171 op_sel:[0,0,1]
	v_pk_fma_f32 v[162:163], v[44:45], s[20:21], v[140:141] op_sel_hi:[1,0,1]
	v_permlane16_swap_b32_e32 v68, v70
	v_permlane16_swap_b32_e32 v69, v71
	s_cmp_le_i32 s96, 128
	s_cbranch_scc1 .Lp7st_5
	global_store_dwordx4 v[156:157], v[68:71], off offset:128
.Lp7st_5:
	v_pk_fma_f32 v[140:141], v[36:37], s[20:21], v[140:141] op_sel_hi:[1,0,1]
	v_pk_fma_f32 v[156:157], v[50:51], s[20:21], v[146:147] op_sel_hi:[1,0,1]
	v_pk_fma_f32 v[70:71], v[48:49], s[20:21], v[144:145] op_sel_hi:[1,0,1]
	v_mov_b32_e32 v68, 0
	v_pk_fma_f32 v[144:145], v[40:41], s[20:21], v[144:145] op_sel_hi:[1,0,1]
	v_cvt_pk_fp8_f32 v68, v70, v71
	v_mov_b32_e32 v69, 0
	v_mov_b32_e32 v70, 0
	v_mov_b32_e32 v71, 0
	v_cvt_pk_fp8_f32 v69, v162, v163
	v_cvt_pk_fp8_f32 v70, v144, v145
	v_cvt_pk_fp8_f32 v71, v140, v141
	v_pk_fma_f32 v[160:161], v[46:47], s[20:21], v[142:143] op_sel_hi:[1,0,1]
	v_pk_fma_f32 v[146:147], v[42:43], s[20:21], v[146:147] op_sel_hi:[1,0,1]
	v_pk_fma_f32 v[142:143], v[38:39], s[20:21], v[142:143] op_sel_hi:[1,0,1]
	v_cvt_pk_fp8_f32 v68, v156, v157 op_sel:[0,0,1]
	v_cvt_pk_fp8_f32 v70, v146, v147 op_sel:[0,0,1]
	v_cvt_pk_fp8_f32 v69, v160, v161 op_sel:[0,0,1]
	v_cvt_pk_fp8_f32 v71, v142, v143 op_sel:[0,0,1]
	v_add_co_u32_e32 v140, vcc, s61, v154
	v_permlane16_swap_b32_e32 v68, v70
	v_permlane16_swap_b32_e32 v69, v71
	v_addc_co_u32_e32 v141, vcc, 0, v155, vcc
	s_cmp_le_i32 s96, 160
	s_cbranch_scc1 .Lp7st_6
	global_store_dwordx4 v[140:141], v[68:71], off
.Lp7st_6:
	v_pk_fma_f32 v[146:147], v[12:13], s[20:21], v[132:133] op_sel_hi:[1,0,1]
	v_pk_fma_f32 v[132:133], v[4:5], s[20:21], v[132:133] op_sel_hi:[1,0,1]
	v_pk_fma_f32 v[70:71], v[16:17], s[20:21], v[136:137] op_sel_hi:[1,0,1]
	v_mov_b32_e32 v68, 0
	v_pk_fma_f32 v[136:137], v[8:9], s[20:21], v[136:137] op_sel_hi:[1,0,1]
	v_cvt_pk_fp8_f32 v68, v70, v71
	v_mov_b32_e32 v69, 0
	v_mov_b32_e32 v70, 0
	v_mov_b32_e32 v71, 0
	v_cvt_pk_fp8_f32 v69, v146, v147
	v_cvt_pk_fp8_f32 v70, v136, v137
	v_cvt_pk_fp8_f32 v71, v132, v133
	v_pk_fma_f32 v[142:143], v[18:19], s[20:21], v[138:139] op_sel_hi:[1,0,1]
	v_pk_fma_f32 v[144:145], v[14:15], s[20:21], v[134:135] op_sel_hi:[1,0,1]
	v_pk_fma_f32 v[138:139], v[10:11], s[20:21], v[138:139] op_sel_hi:[1,0,1]
	v_pk_fma_f32 v[134:135], v[6:7], s[20:21], v[134:135] op_sel_hi:[1,0,1]
	v_cvt_pk_fp8_f32 v68, v142, v143 op_sel:[0,0,1]
	v_cvt_pk_fp8_f32 v70, v138, v139 op_sel:[0,0,1]
	v_cvt_pk_fp8_f32 v69, v144, v145 op_sel:[0,0,1]
	v_cvt_pk_fp8_f32 v71, v134, v135 op_sel:[0,0,1]
	s_andn2_b64 vcc, exec, s[36:37]
	v_permlane16_swap_b32_e32 v68, v70
	v_permlane16_swap_b32_e32 v69, v71
	s_cmp_le_i32 s96, 160
	s_cbranch_scc1 .Lp7st_7
	global_store_dwordx4 v[140:141], v[68:71], off offset:128
.Lp7st_7:
	s_cbranch_vccnz .LBB0_1033
	ds_read_b128 v[0:3], v252
	s_andn2_b64 vcc, exec, s[14:15]
	s_cbranch_vccnz .LBB0_1032
	s_barrier
	s_branch .LBB0_1032
